# in-proj: row-scale loads issued at the top of the last K iteration so the epilogue waits vmcnt(16) instead of draining the next unit's tile prefetch
# speedup vs baseline: 1.0083x; 1.0031x over previous
; #define PG8_STAGE(bufoff, gbase, voff) do { _Pragma("unroll") for (int _i = 0; _i < 2; ++_i) \
;         __builtin_amdgcn_global_load_lds((const unsigned*)((const char*)(gbase) + (voff)[_i]), (PG8_LAS unsigned*)(lds + (bufoff) + ldsw + _i * 8192), 16, 0, 0); } while (0)
; #define PG8_LDA(dst, b, h) do { _Pragma("unroll") for (int m = 0; m < 4; ++m) _Pragma("unroll") for (int k = 0; k < 2; ++k) dst[m][k] = *(const PG8_LAS bf16x8*)(lds + PG8_SA(b, h) + aoff + m * 2048 + k * 1024); } while (0)
; #define PG8_LDB(dst, b, h) do { _Pragma("unroll") for (int n = 0; n < 2; ++n) _Pragma("unroll") for (int k = 0; k < 2; ++k) dst[n][k] = *(const PG8_LAS bf16x8*)(lds + PG8_SB(b, h) + boff + n * 2048 + k * 1024); } while (0)
; #define PG8_WAIT_V(n) asm volatile("s_waitcnt vmcnt(" #n ")" ::: "memory")
; #define PG8_WAIT_L(n) asm volatile("s_waitcnt lgkmcnt(" #n ")" ::: "memory")
; #define PG8_BAR __builtin_amdgcn_s_barrier()
; template <class Epi, class Sched>
; __device__ __forceinline__ void gemm_phase(PG8_LAS unsigned char* lds, const int K, const Sched& S, const Epi& E, const int wave_s) {
;     ...
;             const bool last = (t == nt - 2);
;             const char* a1 = cA + (size_t)(t + 1) * kstepA;
;             const char* a2 = last ? nA : cA + (size_t)(t + 2) * kstepA; const char* b2 = last ? nB : cB + (size_t)(t + 2) * kstepB;
;             const char* a3 = a2 + kstepA; const char* b3 = b2 + kstepB;
;             unsigned v2[2][2];
; #pragma unroll
;             for (int h = 0; h < 2; ++h)
; #pragma unroll
;                 for (int i = 0; i < 2; ++i) v2[h][i] = last ? vN[h][i] : vA[h][i];
;             PG8_LDB(B0, 0, 0); PG8_LDB(B1, 0, 1); PG8_SCHED; PG8_LDA(At, 0, 0); PG8_STAGE(PG8_SA(1, 1), a1, vA[1]);
;             PG8_WAIT_V(8); PG8_WAIT_L(0); PG8_BAR; PG8_MMA(0, 0, At, B0); PG8_MMA(0, 1, At, B1); PG8_BAR; PG8_SCHED;
;             PG8_LDA(At, 0, 1); PG8_STAGE(PG8_SB(0, 0), b2, voffB); PG8_STAGE(PG8_SB(0, 1), b2 + hstepB, voffB); PG8_STAGE(PG8_SA(0, 0), a2, v2[0]);
;             PG8_WAIT_V(8); PG8_WAIT_L(0); PG8_BAR; PG8_MMA(1, 0, At, B0); PG8_MMA(1, 1, At, B1); PG8_BAR; PG8_SCHED;
;     __device__ __forceinline__ void operator()(const f32x4 (&acc)[2][2][4][2], const Unit& u, int wr, int wc, int fr, int fq) const {
;     ...
;             for (int m = 0; m < 4; ++m) rsv[ai][m] = rs ? rs[row0 + ai * HALF + m * 16] : 1.f;
.LBB0_110:
	s_add_u32 s22, s20, 0x100
	s_addc_u32 s23, s21, 0
	s_cmp_eq_u32 s46, 12
	s_cselect_b32 s27, s7, s23
	s_cselect_b32 s26, s6, s22
	s_cselect_b32 s25, s17, s15
	s_cselect_b32 s24, s16, s13
	s_cbranch_scc0 .Linp_nors
	v_lshl_add_u32 v220, s18, 8, v1
	v_ashrrev_i32_e32 v221, 31, v220
	v_lshl_add_u64 v[220:221], v[220:221], 2, s[8:9]
	global_load_dword v246, v[220:221], off
	global_load_dword v247, v[220:221], off offset:64
	global_load_dword v248, v[220:221], off offset:128
	global_load_dword v249, v[220:221], off offset:192
	global_load_dword v250, v[220:221], off offset:512
	global_load_dword v251, v[220:221], off offset:576
	global_load_dword v252, v[220:221], off offset:640
	global_load_dword v253, v[220:221], off offset:704
.Linp_nors:
	s_add_i32 s47, 0, 0x10000
	v_add_u32_e32 v146, s47, v147
	s_add_i32 s48, 0, 0x14000
	ds_read_b128 v[156:159], v146
	ds_read_b128 v[160:163], v146 offset:1024
	ds_read_b128 v[164:167], v146 offset:2048
	ds_read_b128 v[168:171], v146 offset:3072
	v_add_u32_e32 v146, s48, v147
	ds_read_b128 v[172:175], v146
	ds_read_b128 v[176:179], v146 offset:1024
	ds_read_b128 v[180:183], v146 offset:2048
	ds_read_b128 v[192:195], v146 offset:3072
	v_lshl_add_u64 v[148:149], s[20:21], 0, v[144:145]
	s_add_i32 m0, s38, 0xc000
	ds_read_b128 v[196:199], v155
	ds_read_b128 v[200:203], v155 offset:1024
	ds_read_b128 v[222:225], v155 offset:2048
	ds_read_b128 v[226:229], v155 offset:3072
	ds_read_b128 v[230:233], v155 offset:4096
	ds_read_b128 v[234:237], v155 offset:5120
	ds_read_b128 v[238:241], v155 offset:6144
	ds_read_b128 v[242:245], v155 offset:7168
	global_load_lds_dwordx4 v[148:149], off
	v_lshl_add_u64 v[148:149], s[20:21], 0, v[142:143]
	s_add_i32 m0, s38, 0xe000
	s_nop 0
	global_load_lds_dwordx4 v[148:149], off
	s_waitcnt vmcnt(8)
	s_waitcnt lgkmcnt(0)
	s_barrier
	s_setprio 1
	s_waitcnt lgkmcnt(0)
	v_mfma_f32_16x16x32_bf16 v[126:129], v[156:159], v[196:199], v[126:129]
	v_mfma_f32_16x16x32_bf16 v[122:125], v[164:167], v[196:199], v[122:125]
	v_mfma_f32_16x16x32_bf16 v[110:113], v[156:159], v[222:225], v[110:113]
	v_mfma_f32_16x16x32_bf16 v[106:109], v[164:167], v[222:225], v[106:109]
	v_mfma_f32_16x16x32_bf16 v[94:97], v[156:159], v[230:233], v[94:97]
	v_mfma_f32_16x16x32_bf16 v[90:93], v[164:167], v[230:233], v[90:93]
	v_mfma_f32_16x16x32_bf16 v[78:81], v[156:159], v[238:241], v[78:81]
	v_mfma_f32_16x16x32_bf16 v[74:77], v[164:167], v[238:241], v[74:77]
	v_mfma_f32_16x16x32_bf16 v[126:129], v[160:163], v[200:203], v[126:129]
	v_mfma_f32_16x16x32_bf16 v[122:125], v[168:171], v[200:203], v[122:125]
	v_mfma_f32_16x16x32_bf16 v[110:113], v[160:163], v[226:229], v[110:113]
	v_mfma_f32_16x16x32_bf16 v[106:109], v[168:171], v[226:229], v[106:109]
	v_mfma_f32_16x16x32_bf16 v[94:97], v[160:163], v[234:237], v[94:97]
	v_mfma_f32_16x16x32_bf16 v[90:93], v[168:171], v[234:237], v[90:93]
	v_mfma_f32_16x16x32_bf16 v[78:81], v[160:163], v[242:245], v[78:81]
	v_mfma_f32_16x16x32_bf16 v[74:77], v[168:171], v[242:245], v[74:77]
	s_setprio 0
	s_setprio 1
	v_mfma_f32_16x16x32_bf16 v[118:121], v[172:175], v[196:199], v[118:121]
	v_mfma_f32_16x16x32_bf16 v[114:117], v[180:183], v[196:199], v[114:117]
	v_mfma_f32_16x16x32_bf16 v[102:105], v[172:175], v[222:225], v[102:105]
	v_mfma_f32_16x16x32_bf16 v[98:101], v[180:183], v[222:225], v[98:101]
	v_mfma_f32_16x16x32_bf16 v[86:89], v[172:175], v[230:233], v[86:89]
	v_mfma_f32_16x16x32_bf16 v[82:85], v[180:183], v[230:233], v[82:85]
	v_mfma_f32_16x16x32_bf16 v[70:73], v[172:175], v[238:241], v[70:73]
	v_mfma_f32_16x16x32_bf16 v[66:69], v[180:183], v[238:241], v[66:69]
	v_mfma_f32_16x16x32_bf16 v[118:121], v[176:179], v[200:203], v[118:121]
	v_mfma_f32_16x16x32_bf16 v[114:117], v[192:195], v[200:203], v[114:117]
	v_mfma_f32_16x16x32_bf16 v[102:105], v[176:179], v[226:229], v[102:105]
	v_mfma_f32_16x16x32_bf16 v[98:101], v[192:195], v[226:229], v[98:101]
	v_mfma_f32_16x16x32_bf16 v[86:89], v[176:179], v[234:237], v[86:89]
	v_mfma_f32_16x16x32_bf16 v[82:85], v[192:195], v[234:237], v[82:85]
	v_mfma_f32_16x16x32_bf16 v[70:73], v[176:179], v[242:245], v[70:73]
	v_mfma_f32_16x16x32_bf16 v[66:69], v[192:195], v[242:245], v[66:69]
	s_setprio 0
	s_barrier
	s_add_i32 s20, s47, s37
	v_lshl_add_u64 v[148:149], s[24:25], 0, v[132:133]
	s_mov_b32 m0, s20
	ds_read_b128 v[196:199], v155 offset:16384
	ds_read_b128 v[200:203], v155 offset:17408
	ds_read_b128 v[222:225], v155 offset:18432
	ds_read_b128 v[226:229], v155 offset:19456
	ds_read_b128 v[230:233], v155 offset:20480
	ds_read_b128 v[234:237], v155 offset:21504
	ds_read_b128 v[238:241], v155 offset:22528
	ds_read_b128 v[242:245], v155 offset:23552
	global_load_lds_dwordx4 v[148:149], off
	s_add_i32 m0, s20, 0x2000
	s_add_u32 s20, s24, 0x40000
	v_lshl_add_u64 v[152:153], s[24:25], 0, v[130:131]
	s_addc_u32 s21, s25, 0
	s_add_i32 s47, s48, s37
	global_load_lds_dwordx4 v[152:153], off
	v_lshl_add_u64 v[184:185], s[20:21], 0, v[132:133]
	s_mov_b32 m0, s47
	v_lshl_add_u64 v[204:205], s[26:27], 0, v[136:137]
	global_load_lds_dwordx4 v[184:185], off
	v_lshl_add_u64 v[184:185], s[20:21], 0, v[130:131]
	s_add_i32 m0, s47, 0x2000
	s_nop 0
	global_load_lds_dwordx4 v[184:185], off
	v_lshl_add_u64 v[184:185], s[26:27], 0, v[134:135]
	s_mov_b32 m0, s38
	s_nop 0
	global_load_lds_dwordx4 v[184:185], off
	s_mov_b32 m0, s39
	s_nop 0
	global_load_lds_dwordx4 v[204:205], off
	s_waitcnt vmcnt(8)
	s_waitcnt lgkmcnt(0)
	s_barrier
; #define PG8_STAGE(bufoff, gbase, voff) do { _Pragma("unroll") for (int _i = 0; _i < 2; ++_i) \
;         __builtin_amdgcn_global_load_lds((const unsigned*)((const char*)(gbase) + (voff)[_i]), (PG8_LAS unsigned*)(lds + (bufoff) + ldsw + _i * 8192), 16, 0, 0); } while (0)
; #define PG8_LDA(dst, b, h) do { _Pragma("unroll") for (int m = 0; m < 4; ++m) _Pragma("unroll") for (int k = 0; k < 2; ++k) dst[m][k] = *(const PG8_LAS bf16x8*)(lds + PG8_SA(b, h) + aoff + m * 2048 + k * 1024); } while (0)
; #define PG8_LDB(dst, b, h) do { _Pragma("unroll") for (int n = 0; n < 2; ++n) _Pragma("unroll") for (int k = 0; k < 2; ++k) dst[n][k] = *(const PG8_LAS bf16x8*)(lds + PG8_SB(b, h) + boff + n * 2048 + k * 1024); } while (0)
; #define PG8_MMA(ai, bj, At, Bt) do { __builtin_amdgcn_s_setprio(1); _Pragma("unroll") for (int m = 0; m < 4; ++m) _Pragma("unroll") for (int n = 0; n < 2; ++n) _Pragma("unroll") for (int k = 0; k < 2; ++k) \
;         acc[ai][bj][m][n] = __builtin_amdgcn_mfma_f32_16x16x32_bf16(Bt[n][k], At[m][k], acc[ai][bj][m][n], 0, 0, 0); __builtin_amdgcn_s_setprio(0); } while (0)
; #define PG8_WAIT_V(n) asm volatile("s_waitcnt vmcnt(" #n ")" ::: "memory")
; #define PG8_WAIT_L(n) asm volatile("s_waitcnt lgkmcnt(" #n ")" ::: "memory")
; #define PG8_BAR __builtin_amdgcn_s_barrier()
; #define PG8_SCHED __builtin_amdgcn_sched_barrier(0)
; template <class Epi, class Sched>
; __device__ __forceinline__ void gemm_phase(PG8_LAS unsigned char* lds, const int K, const Sched& S, const Epi& E, const int wave_s) {
;     ...
;             PG8_WAIT_V(8); PG8_WAIT_L(0); PG8_BAR; PG8_MMA(1, 0, At, B0); PG8_MMA(1, 1, At, B1); PG8_BAR; PG8_SCHED;
;             PG8_LDB(B0, 1, 0); PG8_LDB(B1, 1, 1); PG8_SCHED; PG8_LDA(At, 1, 0); PG8_STAGE(PG8_SA(0, 1), a2, v2[1]);
;             PG8_WAIT_V(8); PG8_WAIT_L(0); PG8_BAR; PG8_MMA(0, 0, At, B0); PG8_MMA(0, 1, At, B1); PG8_BAR; PG8_SCHED;
	s_setprio 1
	s_waitcnt lgkmcnt(0)
	v_mfma_f32_16x16x32_bf16 v[62:65], v[156:159], v[196:199], v[62:65]
	v_mfma_f32_16x16x32_bf16 v[58:61], v[164:167], v[196:199], v[58:61]
	v_mfma_f32_16x16x32_bf16 v[46:49], v[156:159], v[222:225], v[46:49]
	v_mfma_f32_16x16x32_bf16 v[30:33], v[164:167], v[222:225], v[30:33]
	v_mfma_f32_16x16x32_bf16 v[22:25], v[156:159], v[230:233], v[22:25]
	v_mfma_f32_16x16x32_bf16 v[14:17], v[164:167], v[230:233], v[14:17]
	v_mfma_f32_16x16x32_bf16 v[6:9], v[156:159], v[238:241], v[6:9]
	v_mfma_f32_16x16x32_bf16 v[2:5], v[164:167], v[238:241], v[2:5]
	v_mfma_f32_16x16x32_bf16 v[62:65], v[160:163], v[200:203], v[62:65]
	v_mfma_f32_16x16x32_bf16 v[58:61], v[168:171], v[200:203], v[58:61]
	v_mfma_f32_16x16x32_bf16 v[46:49], v[160:163], v[226:229], v[46:49]
	v_mfma_f32_16x16x32_bf16 v[30:33], v[168:171], v[226:229], v[30:33]
	v_mfma_f32_16x16x32_bf16 v[22:25], v[160:163], v[234:237], v[22:25]
	v_mfma_f32_16x16x32_bf16 v[14:17], v[168:171], v[234:237], v[14:17]
	v_mfma_f32_16x16x32_bf16 v[6:9], v[160:163], v[242:245], v[6:9]
	v_mfma_f32_16x16x32_bf16 v[2:5], v[168:171], v[242:245], v[2:5]
	s_setprio 0
	s_setprio 1
	v_mfma_f32_16x16x32_bf16 v[42:45], v[172:175], v[196:199], v[42:45]
	v_mfma_f32_16x16x32_bf16 v[26:29], v[180:183], v[196:199], v[26:29]
	v_mfma_f32_16x16x32_bf16 v[18:21], v[172:175], v[222:225], v[18:21]
	v_mfma_f32_16x16x32_bf16 v[10:13], v[180:183], v[222:225], v[10:13]
	v_mfma_f32_16x16x32_bf16 v[50:53], v[172:175], v[230:233], v[50:53]
	v_mfma_f32_16x16x32_bf16 v[54:57], v[180:183], v[230:233], v[54:57]
	v_mfma_f32_16x16x32_bf16 v[34:37], v[172:175], v[238:241], v[34:37]
	v_mfma_f32_16x16x32_bf16 v[38:41], v[180:183], v[238:241], v[38:41]
	v_mfma_f32_16x16x32_bf16 v[42:45], v[176:179], v[200:203], v[42:45]
	v_mfma_f32_16x16x32_bf16 v[26:29], v[192:195], v[200:203], v[26:29]
	v_mfma_f32_16x16x32_bf16 v[18:21], v[176:179], v[226:229], v[18:21]
	v_mfma_f32_16x16x32_bf16 v[10:13], v[192:195], v[226:229], v[10:13]
	v_mfma_f32_16x16x32_bf16 v[50:53], v[176:179], v[234:237], v[50:53]
	v_mfma_f32_16x16x32_bf16 v[54:57], v[192:195], v[234:237], v[54:57]
	v_mfma_f32_16x16x32_bf16 v[34:37], v[176:179], v[242:245], v[34:37]
	v_mfma_f32_16x16x32_bf16 v[38:41], v[192:195], v[242:245], v[38:41]
	s_setprio 0
	s_barrier
	s_add_i32 s20, 0, 0x18000
	v_add_u32_e32 v146, s20, v147
	s_add_i32 s47, 0, 0x1c000
	ds_read_b128 v[156:159], v146
	ds_read_b128 v[160:163], v146 offset:1024
	ds_read_b128 v[164:167], v146 offset:2048
	ds_read_b128 v[168:171], v146 offset:3072
	v_add_u32_e32 v146, s47, v147
	ds_read_b128 v[172:175], v146
	ds_read_b128 v[176:179], v146 offset:1024
	ds_read_b128 v[180:183], v146 offset:2048
	ds_read_b128 v[192:195], v146 offset:3072
	s_mov_b32 m0, s40
	v_lshl_add_u64 v[218:219], s[26:27], 0, v[138:139]
	ds_read_b128 v[196:199], v155 offset:32768
	ds_read_b128 v[200:203], v155 offset:33792
	ds_read_b128 v[222:225], v155 offset:34816
	ds_read_b128 v[226:229], v155 offset:35840
	ds_read_b128 v[230:233], v155 offset:36864
	ds_read_b128 v[234:237], v155 offset:37888
	ds_read_b128 v[238:241], v155 offset:38912
	ds_read_b128 v[242:245], v155 offset:39936
	global_load_lds_dwordx4 v[218:219], off
	v_lshl_add_u64 v[218:219], s[26:27], 0, v[140:141]
	s_mov_b32 m0, s41
	s_nop 0
	global_load_lds_dwordx4 v[218:219], off
	s_waitcnt vmcnt(8)
	s_waitcnt lgkmcnt(0)
	s_barrier
	s_setprio 1
	s_waitcnt lgkmcnt(0)
	v_mfma_f32_16x16x32_bf16 v[126:129], v[156:159], v[196:199], v[126:129]
	v_mfma_f32_16x16x32_bf16 v[122:125], v[164:167], v[196:199], v[122:125]
	v_mfma_f32_16x16x32_bf16 v[110:113], v[156:159], v[222:225], v[110:113]
	v_mfma_f32_16x16x32_bf16 v[106:109], v[164:167], v[222:225], v[106:109]
	v_mfma_f32_16x16x32_bf16 v[94:97], v[156:159], v[230:233], v[94:97]
	v_mfma_f32_16x16x32_bf16 v[90:93], v[164:167], v[230:233], v[90:93]
	v_mfma_f32_16x16x32_bf16 v[78:81], v[156:159], v[238:241], v[78:81]
	v_mfma_f32_16x16x32_bf16 v[74:77], v[164:167], v[238:241], v[74:77]
	v_mfma_f32_16x16x32_bf16 v[126:129], v[160:163], v[200:203], v[126:129]
	v_mfma_f32_16x16x32_bf16 v[122:125], v[168:171], v[200:203], v[122:125]
	v_mfma_f32_16x16x32_bf16 v[110:113], v[160:163], v[226:229], v[110:113]
	v_mfma_f32_16x16x32_bf16 v[106:109], v[168:171], v[226:229], v[106:109]
	v_mfma_f32_16x16x32_bf16 v[94:97], v[160:163], v[234:237], v[94:97]
	v_mfma_f32_16x16x32_bf16 v[90:93], v[168:171], v[234:237], v[90:93]
	v_mfma_f32_16x16x32_bf16 v[78:81], v[160:163], v[242:245], v[78:81]
	v_mfma_f32_16x16x32_bf16 v[74:77], v[168:171], v[242:245], v[74:77]
	s_setprio 0
	s_setprio 1
	v_mfma_f32_16x16x32_bf16 v[118:121], v[172:175], v[196:199], v[118:121]
	v_mfma_f32_16x16x32_bf16 v[114:117], v[180:183], v[196:199], v[114:117]
	v_mfma_f32_16x16x32_bf16 v[102:105], v[172:175], v[222:225], v[102:105]
	v_mfma_f32_16x16x32_bf16 v[98:101], v[180:183], v[222:225], v[98:101]
	v_mfma_f32_16x16x32_bf16 v[86:89], v[172:175], v[230:233], v[86:89]
	v_mfma_f32_16x16x32_bf16 v[82:85], v[180:183], v[230:233], v[82:85]
	v_mfma_f32_16x16x32_bf16 v[70:73], v[172:175], v[238:241], v[70:73]
	v_mfma_f32_16x16x32_bf16 v[66:69], v[180:183], v[238:241], v[66:69]
	v_mfma_f32_16x16x32_bf16 v[118:121], v[176:179], v[200:203], v[118:121]
	v_mfma_f32_16x16x32_bf16 v[114:117], v[192:195], v[200:203], v[114:117]
	v_mfma_f32_16x16x32_bf16 v[102:105], v[176:179], v[226:229], v[102:105]
	v_mfma_f32_16x16x32_bf16 v[98:101], v[192:195], v[226:229], v[98:101]
	v_mfma_f32_16x16x32_bf16 v[86:89], v[176:179], v[234:237], v[86:89]
	v_mfma_f32_16x16x32_bf16 v[82:85], v[192:195], v[234:237], v[82:85]
	v_mfma_f32_16x16x32_bf16 v[70:73], v[176:179], v[242:245], v[70:73]
	v_mfma_f32_16x16x32_bf16 v[66:69], v[192:195], v[242:245], v[66:69]
	s_setprio 0
	s_barrier
; #define PG8_STAGE(bufoff, gbase, voff) do { _Pragma("unroll") for (int _i = 0; _i < 2; ++_i) \
;         __builtin_amdgcn_global_load_lds((const unsigned*)((const char*)(gbase) + (voff)[_i]), (PG8_LAS unsigned*)(lds + (bufoff) + ldsw + _i * 8192), 16, 0, 0); } while (0)
; #define PG8_LDA(dst, b, h) do { _Pragma("unroll") for (int m = 0; m < 4; ++m) _Pragma("unroll") for (int k = 0; k < 2; ++k) dst[m][k] = *(const PG8_LAS bf16x8*)(lds + PG8_SA(b, h) + aoff + m * 2048 + k * 1024); } while (0)
; #define PG8_MMA(ai, bj, At, Bt) do { __builtin_amdgcn_s_setprio(1); _Pragma("unroll") for (int m = 0; m < 4; ++m) _Pragma("unroll") for (int n = 0; n < 2; ++n) _Pragma("unroll") for (int k = 0; k < 2; ++k) \
;         acc[ai][bj][m][n] = __builtin_amdgcn_mfma_f32_16x16x32_bf16(Bt[n][k], At[m][k], acc[ai][bj][m][n], 0, 0, 0); __builtin_amdgcn_s_setprio(0); } while (0)
; #define PG8_WAIT_V(n) asm volatile("s_waitcnt vmcnt(" #n ")" ::: "memory")
; #define PG8_WAIT_L(n) asm volatile("s_waitcnt lgkmcnt(" #n ")" ::: "memory")
; #define PG8_BAR __builtin_amdgcn_s_barrier()
; #define PG8_SCHED __builtin_amdgcn_sched_barrier(0)
; template <class Epi, class Sched>
; __device__ __forceinline__ void gemm_phase(PG8_LAS unsigned char* lds, const int K, const Sched& S, const Epi& E, const int wave_s) {
;     ...
;             PG8_WAIT_V(8); PG8_WAIT_L(0); PG8_BAR; PG8_MMA(0, 0, At, B0); PG8_MMA(0, 1, At, B1); PG8_BAR; PG8_SCHED;
;             PG8_LDA(At, 1, 1); PG8_STAGE(PG8_SB(1, 0), b3, voffB); PG8_STAGE(PG8_SB(1, 1), b3 + hstepB, voffB); PG8_STAGE(PG8_SA(1, 0), a3, v2[0]);
;             PG8_WAIT_V(8); PG8_WAIT_L(0); PG8_BAR; PG8_MMA(1, 0, At, B0); PG8_MMA(1, 1, At, B1); PG8_BAR; PG8_SCHED;
;         }
;     __device__ __forceinline__ void operator()(const f32x4 (&acc)[2][2][4][2], const Unit& u, int wr, int wc, int fr, int fq) const {
;     ...
;         for (int ai = 0; ai < 2; ++ai)
; #pragma unroll
;             for (int m = 0; m < 4; ++m) rsv[ai][m] = rs ? rs[row0 + ai * HALF + m * 16] : 1.f;
;         f32x4 bv[2][2];
; #pragma unroll
;         for (int bj = 0; bj < 2; ++bj)
; #pragma unroll
;             for (int n = 0; n < 2; ++n) bv[bj][n] = bs ? *(const f32x4*)(bs + col0 + bj * HALF + 4 * n) : (f32x4){0.f, 0.f, 0.f, 0.f};
	s_add_i32 s20, s20, s37
	v_lshl_add_u64 v[148:149], v[148:149], 0, s[60:61]
	s_mov_b32 m0, s20
	ds_read_b128 v[196:199], v155 offset:49152
	ds_read_b128 v[200:203], v155 offset:50176
	ds_read_b128 v[222:225], v155 offset:51200
	ds_read_b128 v[226:229], v155 offset:52224
	ds_read_b128 v[230:233], v155 offset:53248
	ds_read_b128 v[234:237], v155 offset:54272
	ds_read_b128 v[238:241], v155 offset:55296
	ds_read_b128 v[242:245], v155 offset:56320
	global_load_lds_dwordx4 v[148:149], off
	s_add_i32 m0, s20, 0x2000
	s_add_u32 s20, s24, 0x40080
	v_lshl_add_u64 v[148:149], v[152:153], 0, s[60:61]
	s_addc_u32 s21, s25, 0
	s_add_i32 s24, s47, s37
	global_load_lds_dwordx4 v[148:149], off
	v_lshl_add_u64 v[148:149], s[20:21], 0, v[132:133]
	s_mov_b32 m0, s24
	s_nop 0
	global_load_lds_dwordx4 v[148:149], off
	v_lshl_add_u64 v[148:149], s[20:21], 0, v[130:131]
	s_add_i32 m0, s24, 0x2000
	s_nop 0
	global_load_lds_dwordx4 v[148:149], off
	v_lshl_add_u64 v[148:149], v[184:185], 0, s[60:61]
	s_mov_b32 m0, s43
	s_nop 0
	global_load_lds_dwordx4 v[148:149], off
	v_lshl_add_u64 v[148:149], v[204:205], 0, s[60:61]
	s_mov_b32 m0, s44
	s_nop 0
	global_load_lds_dwordx4 v[148:149], off
	s_waitcnt vmcnt(8)
	s_waitcnt lgkmcnt(0)
	s_barrier
	s_setprio 1
	s_waitcnt lgkmcnt(0)
	v_mfma_f32_16x16x32_bf16 v[62:65], v[156:159], v[196:199], v[62:65]
	v_mfma_f32_16x16x32_bf16 v[58:61], v[164:167], v[196:199], v[58:61]
	v_mfma_f32_16x16x32_bf16 v[46:49], v[156:159], v[222:225], v[46:49]
	v_mfma_f32_16x16x32_bf16 v[30:33], v[164:167], v[222:225], v[30:33]
	v_mfma_f32_16x16x32_bf16 v[22:25], v[156:159], v[230:233], v[22:25]
	v_mfma_f32_16x16x32_bf16 v[14:17], v[164:167], v[230:233], v[14:17]
	v_mfma_f32_16x16x32_bf16 v[6:9], v[156:159], v[238:241], v[6:9]
	v_mfma_f32_16x16x32_bf16 v[2:5], v[164:167], v[238:241], v[2:5]
	v_mfma_f32_16x16x32_bf16 v[62:65], v[160:163], v[200:203], v[62:65]
	v_mfma_f32_16x16x32_bf16 v[58:61], v[168:171], v[200:203], v[58:61]
	v_mfma_f32_16x16x32_bf16 v[46:49], v[160:163], v[226:229], v[46:49]
	v_mfma_f32_16x16x32_bf16 v[30:33], v[168:171], v[226:229], v[30:33]
	v_mfma_f32_16x16x32_bf16 v[22:25], v[160:163], v[234:237], v[22:25]
	v_mfma_f32_16x16x32_bf16 v[14:17], v[168:171], v[234:237], v[14:17]
	v_mfma_f32_16x16x32_bf16 v[6:9], v[160:163], v[242:245], v[6:9]
	v_mfma_f32_16x16x32_bf16 v[2:5], v[168:171], v[242:245], v[2:5]
	s_setprio 0
	s_setprio 1
	v_mfma_f32_16x16x32_bf16 v[42:45], v[172:175], v[196:199], v[42:45]
	v_mfma_f32_16x16x32_bf16 v[26:29], v[180:183], v[196:199], v[26:29]
	v_mfma_f32_16x16x32_bf16 v[18:21], v[172:175], v[222:225], v[18:21]
	v_mfma_f32_16x16x32_bf16 v[10:13], v[180:183], v[222:225], v[10:13]
	v_mfma_f32_16x16x32_bf16 v[50:53], v[172:175], v[230:233], v[50:53]
	v_mfma_f32_16x16x32_bf16 v[54:57], v[180:183], v[230:233], v[54:57]
	v_mfma_f32_16x16x32_bf16 v[34:37], v[172:175], v[238:241], v[34:37]
	v_mfma_f32_16x16x32_bf16 v[38:41], v[180:183], v[238:241], v[38:41]
	v_mfma_f32_16x16x32_bf16 v[42:45], v[176:179], v[200:203], v[42:45]
	v_mfma_f32_16x16x32_bf16 v[26:29], v[192:195], v[200:203], v[26:29]
	v_mfma_f32_16x16x32_bf16 v[18:21], v[176:179], v[226:229], v[18:21]
	v_mfma_f32_16x16x32_bf16 v[10:13], v[192:195], v[226:229], v[10:13]
	v_mfma_f32_16x16x32_bf16 v[50:53], v[176:179], v[234:237], v[50:53]
	v_mfma_f32_16x16x32_bf16 v[54:57], v[192:195], v[234:237], v[54:57]
	v_mfma_f32_16x16x32_bf16 v[34:37], v[176:179], v[242:245], v[34:37]
	v_mfma_f32_16x16x32_bf16 v[38:41], v[192:195], v[242:245], v[38:41]
	s_setprio 0
	s_barrier
	s_add_i32 s46, s46, 2
	s_add_u32 s13, s13, 0x100
	s_addc_u32 s15, s15, 0
	s_cmp_gt_u32 s46, 13
	s_mov_b64 s[20:21], s[22:23]
	s_cbranch_scc0 .LBB0_110
	s_and_b64 vcc, exec, s[10:11]
	s_cbranch_vccz .LBB0_113
	s_barrier
.LBB0_113:
	v_lshl_add_u32 v148, s18, 8, v1
	v_ashrrev_i32_e32 v149, 31, v148
	v_lshl_add_u64 v[162:163], v[148:149], 2, s[8:9]
	v_lshl_or_b32 v152, s19, 8, v151
	v_ashrrev_i32_e32 v153, 31, v152
	v_lshl_add_u64 v[152:153], v[152:153], 1, s[2:3]
	v_mad_i64_i32 v[162:163], s[18:19], v148, s88, v[152:153]
	v_add_u32_e32 v149, 0x80, v148
	s_and_b64 vcc, exec, s[4:5]
	s_waitcnt vmcnt(16)
	v_mov_b32_e32 v164, v246
	v_mov_b32_e32 v166, v247
	v_mov_b32_e32 v160, v248
	v_mov_b32_e32 v158, v249
	v_mov_b32_e32 v156, v250
	v_mov_b32_e32 v154, v251
	v_mov_b32_e32 v150, v252
	v_mov_b32_e32 v146, v253
	v_pk_fma_f32 v[128:129], v[128:129], v[164:165], 0 op_sel_hi:[1,0,0]
	v_pk_fma_f32 v[126:127], v[126:127], v[164:165], 0 op_sel_hi:[1,0,0]
	v_pk_fma_f32 v[168:169], v[124:125], v[164:165], 0 op_sel_hi:[1,0,0]
	v_pk_fma_f32 v[124:125], v[122:123], v[164:165], 0 op_sel_hi:[1,0,0]
	v_cvt_pk_bf16_f32 v122, v126, v127
	v_cvt_pk_bf16_f32 v123, v128, v129
	v_cvt_pk_bf16_f32 v124, v124, v125
	v_cvt_pk_bf16_f32 v125, v168, v169
	global_store_dwordx4 v[162:163], v[122:125], off
	v_pk_fma_f32 v[120:121], v[120:121], v[164:165], 0 op_sel_hi:[1,0,0]
	v_pk_fma_f32 v[118:119], v[118:119], v[164:165], 0 op_sel_hi:[1,0,0]
	v_pk_fma_f32 v[122:123], v[116:117], v[164:165], 0 op_sel_hi:[1,0,0]
	v_pk_fma_f32 v[116:117], v[114:115], v[164:165], 0 op_sel_hi:[1,0,0]
	v_cvt_pk_bf16_f32 v114, v118, v119
	v_cvt_pk_bf16_f32 v115, v120, v121
	v_cvt_pk_bf16_f32 v116, v116, v117
	v_cvt_pk_bf16_f32 v117, v122, v123
	global_store_dwordx4 v[162:163], v[114:117], off offset:256
	v_pk_fma_f32 v[112:113], v[112:113], v[166:167], 0 op_sel_hi:[1,0,0]
	v_pk_fma_f32 v[110:111], v[110:111], v[166:167], 0 op_sel_hi:[1,0,0]
	v_or_b32_e32 v114, 16, v148
	v_pk_fma_f32 v[116:117], v[108:109], v[166:167], 0 op_sel_hi:[1,0,0]
	v_pk_fma_f32 v[108:109], v[106:107], v[166:167], 0 op_sel_hi:[1,0,0]
	v_mad_i64_i32 v[114:115], s[18:19], v114, s88, v[152:153]
; __device__ __forceinline__ float fsigmoid(float x) { return __builtin_amdgcn_rcpf(1.f + __builtin_amdgcn_exp2f(-x * LOG2E)); }
; __device__ __forceinline__ float fgelu(float x) { const float y = 1.5957691216057308f * (x + 0.044715f * x * x * x); return x * __builtin_amdgcn_rcpf(1.f + __builtin_amdgcn_exp2f(-y * LOG2E)); }
; __device__ __forceinline__ unsigned cvt_pk_bf16(float lo, float hi) { return pk2(lo, hi); }
;     __device__ __forceinline__ void operator()(const f32x4 (&acc)[2][2][4][2], const Unit& u, int wr, int wc, int fr, int fq) const {
;     ...
;         for (int ai = 0; ai < 2; ++ai)
; #pragma unroll
;             for (int m = 0; m < 4; ++m) { bf16_t* rowp = base + (size_t)(row0 + ai * HALF + m * 16) * ldc + col0; const float sc = rsv[ai][m];
; #pragma unroll
;                 for (int bj = 0; bj < 2; ++bj) { f32x4 v0 = acc[ai][bj][m][0], v1 = acc[ai][bj][m][1];
;                     if (rs) { v0 *= sc; v1 *= sc; }
;                     v0 += bv[bj][0]; v1 += bv[bj][1];
;                     if (ACT == 1) { for (int e = 0; e < 4; ++e) { v0[e] = fgelu(v0[e]); v1[e] = fgelu(v1[e]); } }
;                     if (ACT == 2) { for (int e = 0; e < 4; ++e) { v0[e] = fsigmoid(v0[e]); v1[e] = fsigmoid(v1[e]); } }
;                     u32x4 w; w.x = cvt_pk_bf16(v0[0], v0[1]); w.y = cvt_pk_bf16(v0[2], v0[3]); w.z = cvt_pk_bf16(v1[0], v1[1]); w.w = cvt_pk_bf16(v1[2], v1[3]);
;                     *(u32x4*)(rowp + bj * HALF) = w; } }
	v_cvt_pk_bf16_f32 v106, v110, v111
	v_cvt_pk_bf16_f32 v107, v112, v113
	v_cvt_pk_bf16_f32 v108, v108, v109
	v_cvt_pk_bf16_f32 v109, v116, v117
	global_store_dwordx4 v[114:115], v[106:109], off
	v_pk_fma_f32 v[104:105], v[104:105], v[166:167], 0 op_sel_hi:[1,0,0]
	v_pk_fma_f32 v[102:103], v[102:103], v[166:167], 0 op_sel_hi:[1,0,0]
	v_pk_fma_f32 v[106:107], v[100:101], v[166:167], 0 op_sel_hi:[1,0,0]
	v_pk_fma_f32 v[100:101], v[98:99], v[166:167], 0 op_sel_hi:[1,0,0]
	v_cvt_pk_bf16_f32 v98, v102, v103
	v_cvt_pk_bf16_f32 v99, v104, v105
	v_cvt_pk_bf16_f32 v100, v100, v101
	v_cvt_pk_bf16_f32 v101, v106, v107
	global_store_dwordx4 v[114:115], v[98:101], off offset:256
	v_pk_fma_f32 v[96:97], v[96:97], v[160:161], 0 op_sel_hi:[1,0,0]
	v_pk_fma_f32 v[94:95], v[94:95], v[160:161], 0 op_sel_hi:[1,0,0]
	v_or_b32_e32 v98, 32, v148
	v_pk_fma_f32 v[100:101], v[92:93], v[160:161], 0 op_sel_hi:[1,0,0]
	v_pk_fma_f32 v[92:93], v[90:91], v[160:161], 0 op_sel_hi:[1,0,0]
	v_mad_i64_i32 v[98:99], s[18:19], v98, s88, v[152:153]
	v_cvt_pk_bf16_f32 v90, v94, v95
	v_cvt_pk_bf16_f32 v91, v96, v97
	v_cvt_pk_bf16_f32 v92, v92, v93
	v_cvt_pk_bf16_f32 v93, v100, v101
	global_store_dwordx4 v[98:99], v[90:93], off
	v_pk_fma_f32 v[88:89], v[88:89], v[160:161], 0 op_sel_hi:[1,0,0]
	v_pk_fma_f32 v[86:87], v[86:87], v[160:161], 0 op_sel_hi:[1,0,0]
	v_pk_fma_f32 v[90:91], v[84:85], v[160:161], 0 op_sel_hi:[1,0,0]
	v_pk_fma_f32 v[84:85], v[82:83], v[160:161], 0 op_sel_hi:[1,0,0]
	v_cvt_pk_bf16_f32 v82, v86, v87
	v_cvt_pk_bf16_f32 v83, v88, v89
	v_cvt_pk_bf16_f32 v84, v84, v85
	v_cvt_pk_bf16_f32 v85, v90, v91
	global_store_dwordx4 v[98:99], v[82:85], off offset:256
	v_pk_fma_f32 v[80:81], v[80:81], v[158:159], 0 op_sel_hi:[1,0,0]
	v_pk_fma_f32 v[78:79], v[78:79], v[158:159], 0 op_sel_hi:[1,0,0]
	v_or_b32_e32 v82, 48, v148
	v_pk_fma_f32 v[84:85], v[76:77], v[158:159], 0 op_sel_hi:[1,0,0]
	v_pk_fma_f32 v[76:77], v[74:75], v[158:159], 0 op_sel_hi:[1,0,0]
	v_mad_i64_i32 v[82:83], s[18:19], v82, s88, v[152:153]
	v_cvt_pk_bf16_f32 v74, v78, v79
	v_cvt_pk_bf16_f32 v75, v80, v81
	v_cvt_pk_bf16_f32 v76, v76, v77
	v_cvt_pk_bf16_f32 v77, v84, v85
	global_store_dwordx4 v[82:83], v[74:77], off
	v_pk_fma_f32 v[72:73], v[72:73], v[158:159], 0 op_sel_hi:[1,0,0]
	v_pk_fma_f32 v[70:71], v[70:71], v[158:159], 0 op_sel_hi:[1,0,0]
	v_pk_fma_f32 v[74:75], v[68:69], v[158:159], 0 op_sel_hi:[1,0,0]
	v_pk_fma_f32 v[68:69], v[66:67], v[158:159], 0 op_sel_hi:[1,0,0]
	v_cvt_pk_bf16_f32 v66, v70, v71
	v_cvt_pk_bf16_f32 v67, v72, v73
	v_cvt_pk_bf16_f32 v68, v68, v69
	v_cvt_pk_bf16_f32 v69, v74, v75
	global_store_dwordx4 v[82:83], v[66:69], off offset:256
	v_pk_fma_f32 v[64:65], v[64:65], v[156:157], 0 op_sel_hi:[1,0,0]
	v_pk_fma_f32 v[62:63], v[62:63], v[156:157], 0 op_sel_hi:[1,0,0]
	v_pk_fma_f32 v[68:69], v[60:61], v[156:157], 0 op_sel_hi:[1,0,0]
	v_pk_fma_f32 v[60:61], v[58:59], v[156:157], 0 op_sel_hi:[1,0,0]
	v_mad_i64_i32 v[66:67], s[18:19], v149, s88, v[152:153]
	v_cvt_pk_bf16_f32 v58, v62, v63
	v_cvt_pk_bf16_f32 v59, v64, v65
	v_cvt_pk_bf16_f32 v60, v60, v61
	v_cvt_pk_bf16_f32 v61, v68, v69
	global_store_dwordx4 v[66:67], v[58:61], off
	v_pk_fma_f32 v[44:45], v[44:45], v[156:157], 0 op_sel_hi:[1,0,0]
	v_pk_fma_f32 v[42:43], v[42:43], v[156:157], 0 op_sel_hi:[1,0,0]
	v_pk_fma_f32 v[58:59], v[28:29], v[156:157], 0 op_sel_hi:[1,0,0]
	v_pk_fma_f32 v[28:29], v[26:27], v[156:157], 0 op_sel_hi:[1,0,0]
	v_cvt_pk_bf16_f32 v26, v42, v43
	v_cvt_pk_bf16_f32 v27, v44, v45
	v_cvt_pk_bf16_f32 v28, v28, v29
	v_cvt_pk_bf16_f32 v29, v58, v59
	global_store_dwordx4 v[66:67], v[26:29], off offset:256
	v_pk_fma_f32 v[32:33], v[32:33], v[154:155], 0 op_sel_hi:[1,0,0]
	v_pk_fma_f32 v[30:31], v[30:31], v[154:155], 0 op_sel_hi:[1,0,0]
	v_add_u32_e32 v26, 0x90, v148
	v_mad_i64_i32 v[42:43], s[18:19], v26, s88, v[152:153]
	v_pk_fma_f32 v[28:29], v[48:49], v[154:155], 0 op_sel_hi:[1,0,0]
	v_pk_fma_f32 v[26:27], v[46:47], v[154:155], 0 op_sel_hi:[1,0,0]
	v_pk_fma_f32 v[20:21], v[20:21], v[154:155], 0 op_sel_hi:[1,0,0]
	v_cvt_pk_bf16_f32 v26, v26, v27
	v_cvt_pk_bf16_f32 v27, v28, v29
	v_cvt_pk_bf16_f32 v28, v30, v31
	v_cvt_pk_bf16_f32 v29, v32, v33
	global_store_dwordx4 v[42:43], v[26:29], off
	v_pk_fma_f32 v[18:19], v[18:19], v[154:155], 0 op_sel_hi:[1,0,0]
	v_pk_fma_f32 v[16:17], v[16:17], v[150:151], 0 op_sel_hi:[1,0,0]
	v_pk_fma_f32 v[26:27], v[12:13], v[154:155], 0 op_sel_hi:[1,0,0]
	v_pk_fma_f32 v[12:13], v[10:11], v[154:155], 0 op_sel_hi:[1,0,0]
	v_cvt_pk_bf16_f32 v10, v18, v19
	v_cvt_pk_bf16_f32 v11, v20, v21
	v_cvt_pk_bf16_f32 v12, v12, v13
	v_cvt_pk_bf16_f32 v13, v26, v27
	global_store_dwordx4 v[42:43], v[10:13], off offset:256
	v_pk_fma_f32 v[14:15], v[14:15], v[150:151], 0 op_sel_hi:[1,0,0]
	v_pk_fma_f32 v[8:9], v[8:9], v[146:147], 0 op_sel_hi:[1,0,0]
	v_add_u32_e32 v10, 0xa0, v148
	v_mad_i64_i32 v[18:19], s[18:19], v10, s88, v[152:153]
	v_pk_fma_f32 v[12:13], v[24:25], v[150:151], 0 op_sel_hi:[1,0,0]
	v_pk_fma_f32 v[10:11], v[22:23], v[150:151], 0 op_sel_hi:[1,0,0]
	v_pk_fma_f32 v[6:7], v[6:7], v[146:147], 0 op_sel_hi:[1,0,0]
	v_cvt_pk_bf16_f32 v10, v10, v11
	v_cvt_pk_bf16_f32 v11, v12, v13
	v_cvt_pk_bf16_f32 v12, v14, v15
	v_cvt_pk_bf16_f32 v13, v16, v17
	global_store_dwordx4 v[18:19], v[10:13], off
	v_pk_fma_f32 v[14:15], v[56:57], v[150:151], 0 op_sel_hi:[1,0,0]
	v_pk_fma_f32 v[16:17], v[54:55], v[150:151], 0 op_sel_hi:[1,0,0]
	v_pk_fma_f32 v[12:13], v[52:53], v[150:151], 0 op_sel_hi:[1,0,0]
	v_pk_fma_f32 v[10:11], v[50:51], v[150:151], 0 op_sel_hi:[1,0,0]
	s_nop 0
	v_cvt_pk_bf16_f32 v10, v10, v11
	v_cvt_pk_bf16_f32 v11, v12, v13
	v_cvt_pk_bf16_f32 v12, v16, v17
	v_cvt_pk_bf16_f32 v13, v14, v15
	global_store_dwordx4 v[18:19], v[10:13], off offset:256
	s_nop 1
	v_add_u32_e32 v10, 0xb0, v148
	v_pk_fma_f32 v[12:13], v[4:5], v[146:147], 0 op_sel_hi:[1,0,0]
	v_pk_fma_f32 v[4:5], v[2:3], v[146:147], 0 op_sel_hi:[1,0,0]
	v_mad_i64_i32 v[10:11], s[18:19], v10, s88, v[152:153]
	v_cvt_pk_bf16_f32 v2, v6, v7
	v_cvt_pk_bf16_f32 v3, v8, v9
	v_cvt_pk_bf16_f32 v4, v4, v5
	v_cvt_pk_bf16_f32 v5, v12, v13
	global_store_dwordx4 v[10:11], v[2:5], off
	v_pk_fma_f32 v[6:7], v[40:41], v[146:147], 0 op_sel_hi:[1,0,0]
	v_pk_fma_f32 v[8:9], v[38:39], v[146:147], 0 op_sel_hi:[1,0,0]
	v_pk_fma_f32 v[4:5], v[36:37], v[146:147], 0 op_sel_hi:[1,0,0]
	v_pk_fma_f32 v[2:3], v[34:35], v[146:147], 0 op_sel_hi:[1,0,0]
	s_mov_b64 s[18:19], -1
	v_cvt_pk_bf16_f32 v2, v2, v3
	v_cvt_pk_bf16_f32 v3, v4, v5
	v_cvt_pk_bf16_f32 v4, v8, v9
	v_cvt_pk_bf16_f32 v5, v6, v7
	global_store_dwordx4 v[10:11], v[2:5], off offset:256
	s_cbranch_vccnz .LBB0_104
	s_andn2_b64 vcc, exec, s[0:1]
	s_cbranch_vccnz .LBB0_103
	s_barrier
	s_branch .LBB0_103
